# P2 stages G/H: second round's LDS reads issued with the first round's ahead of the MFMAs (counted lgkmcnt); stacked on stage I pipelining
# speedup vs baseline: 1.0011x; 1.0011x over previous
.LBB0_456:
	s_waitcnt lgkmcnt(0)
	s_barrier
	s_add_i32 s10, 0, 0x8000
	v_bfe_u32 v1, v186, 5, 1
	v_lshl_or_b32 v2, v1, 2, s4
	v_or_b32_e32 v211, 8, v2
	v_lshlrev_b32_e32 v4, 2, v2
	v_lshlrev_b32_e32 v8, 2, v211
	v_or_b32_e32 v214, 16, v2
	v_or_b32_e32 v216, 24, v2
	v_add_u32_e32 v5, s67, v4
	v_add_u32_e32 v6, s82, v4
	v_add_u32_e32 v4, s83, v4
	v_add_u32_e32 v9, s67, v8
	v_lshlrev_b32_e32 v12, 2, v214
	v_lshlrev_b32_e32 v16, 2, v216
	ds_read_b128 v[154:157], v5
	ds_read_b128 v[158:161], v6
	ds_read_b128 v[4:7], v4
	ds_read_b128 v[162:165], v9
	v_add_u32_e32 v9, s82, v8
	v_add_u32_e32 v8, s83, v8
	v_add_u32_e32 v13, s67, v12
	v_add_u32_e32 v14, s82, v12
	v_add_u32_e32 v12, s83, v12
	v_add_u32_e32 v17, s67, v16
	ds_read_b128 v[166:169], v9
	ds_read_b128 v[8:11], v8
	ds_read_b128 v[170:173], v13
	ds_read_b128 v[174:177], v14
	ds_read_b128 v[12:15], v12
	ds_read_b128 v[178:181], v17
	v_add_u32_e32 v17, s82, v16
	v_add_u32_e32 v16, s83, v16
	ds_read_b128 v[182:185], v17
	ds_read_b128 v[150:153], v16
	v_lshrrev_b32_e32 v16, 3, v186
	v_bfe_u32 v217, v186, 2, 2
	v_and_b32_e32 v16, 2, v16
	v_bfe_u32 v17, v186, 1, 1
	v_or3_b32 v218, v16, s5, v17
	v_lshlrev_b32_e32 v219, 2, v217
	v_lshlrev_b32_e32 v16, 3, v186
	v_and_or_b32 v220, v16, 8, s10
	v_bitop3_b32 v16, v219, v218, v1 bitop3:0x36
	v_or_b32_e32 v2, v2, v217
	v_lshl_add_u32 v215, v16, 4, v220
	v_lshl_add_u32 v2, v2, 8, v215
	ds_read_b64_tr_b16 v[16:17], v2
	v_or_b32_e32 v2, v211, v217
	v_bfe_u32 v211, v211, 2, 2
	v_bitop3_b32 v211, v211, v218, v219 bitop3:0x36
	v_lshlrev_b32_e32 v2, 8, v2
	v_lshlrev_b32_e32 v211, 4, v211
	v_add3_u32 v2, v2, v220, v211
	ds_read_b64_tr_b16 v[212:213], v2
	v_or_b32_e32 v2, v214, v217
	v_lshl_add_u32 v2, v2, 8, v215
	v_bfe_u32 v211, v216, 2, 2
	ds_read_b64_tr_b16 v[214:215], v2
	v_or_b32_e32 v2, v216, v217
	v_bitop3_b32 v211, v211, v218, v219 bitop3:0x36
	v_lshlrev_b32_e32 v2, 8, v2
	v_lshlrev_b32_e32 v211, 4, v211
	v_add3_u32 v2, v2, v220, v211
	ds_read_b64_tr_b16 v[216:217], v2
	s_waitcnt lgkmcnt(0)
	v_and_b32_e32 v219, 0xffff0000, v16
	v_lshlrev_b32_e32 v218, 16, v16
	s_waitcnt lgkmcnt(10)
	v_pk_fma_f32 v[66:67], v[66:67], v[158:159], v[218:219] neg_lo:[1,0,0] neg_hi:[1,0,0]
	v_and_or_b32 v2, v186, 31, s17
	v_pk_mul_f32 v[66:67], v[154:155], v[66:67]
	v_and_b32_e32 v155, 0xffff0000, v17
	v_lshlrev_b32_e32 v154, 16, v17
	v_pk_fma_f32 v[16:17], v[68:69], v[160:161], v[154:155] neg_lo:[1,0,0] neg_hi:[1,0,0]
	v_and_b32_e32 v69, 0xffff0000, v212
	v_lshlrev_b32_e32 v68, 16, v212
	v_lshlrev_b32_e32 v2, 7, v2
	v_lshlrev_b32_e32 v1, 3, v1
	v_pk_mul_f32 v[16:17], v[156:157], v[16:17]
	s_waitcnt lgkmcnt(7)
	v_pk_fma_f32 v[68:69], v[70:71], v[166:167], v[68:69] neg_lo:[1,0,0] neg_hi:[1,0,0]
	v_and_b32_e32 v71, 0xffff0000, v213
	v_lshlrev_b32_e32 v70, 16, v213
	v_add3_u32 v1, s18, v2, v1
	v_bitop3_b32 v2, v186, s40, 7 bitop3:0x6c
	v_pk_fma_f32 v[70:71], v[72:73], v[168:169], v[70:71] neg_lo:[1,0,0] neg_hi:[1,0,0]
	v_and_b32_e32 v73, 0xffff0000, v214
	v_lshlrev_b32_e32 v72, 16, v214
	v_cvt_pk_bf16_f32 v66, v66, v67
	v_cvt_pk_bf16_f32 v67, v16, v17
	v_lshl_add_u32 v2, v2, 4, v1
	v_pk_mul_f32 v[68:69], v[162:163], v[68:69]
	v_pk_mul_f32 v[70:71], v[164:165], v[70:71]
	s_waitcnt lgkmcnt(4)
	v_pk_fma_f32 v[72:73], v[74:75], v[174:175], v[72:73] neg_lo:[1,0,0] neg_hi:[1,0,0]
	v_and_b32_e32 v75, 0xffff0000, v215
	v_lshlrev_b32_e32 v74, 16, v215
	ds_write_b64 v2, v[66:67]
	v_bitop3_b32 v2, v186, s65, 7 bitop3:0x6c
	v_pk_fma_f32 v[74:75], v[76:77], v[176:177], v[74:75] neg_lo:[1,0,0] neg_hi:[1,0,0]
	v_and_b32_e32 v77, 0xffff0000, v216
	v_lshlrev_b32_e32 v76, 16, v216
	v_cvt_pk_bf16_f32 v16, v68, v69
	v_cvt_pk_bf16_f32 v17, v70, v71
	v_lshl_add_u32 v2, v2, 4, v1
	v_pk_mul_f32 v[72:73], v[170:171], v[72:73]
	v_pk_mul_f32 v[74:75], v[172:173], v[74:75]
	s_waitcnt lgkmcnt(2)
	v_pk_fma_f32 v[76:77], v[78:79], v[182:183], v[76:77] neg_lo:[1,0,0] neg_hi:[1,0,0]
	v_and_b32_e32 v79, 0xffff0000, v217
	v_lshlrev_b32_e32 v78, 16, v217
	ds_write_b64 v2, v[16:17]
	v_bitop3_b32 v2, v186, s33, 7 bitop3:0x6c
	v_pk_fma_f32 v[78:79], v[80:81], v[184:185], v[78:79] neg_lo:[1,0,0] neg_hi:[1,0,0]
	v_cvt_pk_bf16_f32 v16, v72, v73
	v_cvt_pk_bf16_f32 v17, v74, v75
	v_lshl_add_u32 v2, v2, 4, v1
	v_pk_mul_f32 v[76:77], v[178:179], v[76:77]
	v_pk_mul_f32 v[78:79], v[180:181], v[78:79]
	ds_write_b64 v2, v[16:17]
	v_bitop3_b32 v2, v186, s2, 7 bitop3:0x6c
	v_cvt_pk_bf16_f32 v16, v76, v77
	v_cvt_pk_bf16_f32 v17, v78, v79
	v_lshl_add_u32 v1, v2, 4, v1
	ds_write_b64 v1, v[16:17]
	s_waitcnt lgkmcnt(0)
	s_barrier
	s_nop 0
	v_and_b32_e32 v1, 31, v186
	v_lshrrev_b32_e32 v66, 5, v186
	v_and_b32_e32 v2, 7, v186
	v_lshl_add_u32 v154, v1, 7, s27
	v_or_b32_e32 v1, s17, v1
	v_lshlrev_b32_e32 v16, 7, v1
	v_bitop3_b32 v1, v66, v2, 1 bitop3:0x6c
	v_add_u32_e32 v155, s18, v16
	v_lshlrev_b32_e32 v1, 4, v1
	v_bfe_u32 v17, v186, 5, 1
	v_add_u32_e32 v66, v154, v1
	v_add_u32_e32 v1, v155, v1
	ds_read_b128 v[66:69], v66
	ds_read_b128 v[70:73], v1
	v_bitop3_b32 v1, v17, v2, 2 bitop3:0x36
	v_lshlrev_b32_e32 v1, 4, v1
	v_add_u32_e32 v74, v154, v1
	v_add_u32_e32 v1, v155, v1
	ds_read_b128 v[156:159], v74
	ds_read_b128 v[160:163], v1
	s_and_b64 vcc, exec, s[14:15]
	s_cbranch_vccnz .Lp2g_notb
	v_bitop3_b32 v1, v17, v2, 4 bitop3:0x36
	v_lshlrev_b32_e32 v1, 4, v1
	v_add_u32_e32 v252, v154, v1
	v_add_u32_e32 v1, v155, v1
	ds_read_b128 v[244:247], v252
	ds_read_b128 v[248:251], v1
	v_bitop3_b32 v1, v17, v2, 6 bitop3:0x36
	v_lshlrev_b32_e32 v1, 4, v1
	v_add_u32_e32 v252, v154, v1
	v_add_u32_e32 v1, v155, v1
	ds_read_b128 v[164:167], v252
	ds_read_b128 v[168:171], v1
	s_waitcnt lgkmcnt(6)
	v_mfma_f32_32x32x16_bf16 v[66:81], v[66:69], v[70:73], 0
	s_waitcnt lgkmcnt(4)
	v_mfma_f32_32x32x16_bf16 v[66:81], v[156:159], v[160:163], v[66:81]
	s_waitcnt lgkmcnt(2)
	v_mfma_f32_32x32x16_bf16 v[66:81], v[244:247], v[248:251], v[66:81]
	s_waitcnt lgkmcnt(0)
	v_mfma_f32_32x32x16_bf16 v[66:81], v[164:167], v[168:171], v[66:81]
	s_branch .LBB0_458
.Lp2g_notb:
	s_waitcnt lgkmcnt(2)
	v_mfma_f32_32x32x16_bf16 v[66:81], v[66:69], v[70:73], 0
	s_waitcnt lgkmcnt(0)
	v_mfma_f32_32x32x16_bf16 v[66:81], v[156:159], v[160:163], v[66:81]
.LBB0_458:
	v_lshl_add_u32 v1, v17, 4, s35
	ds_read_b128 v[154:157], v1
	ds_read_b128 v[158:161], v1 offset:32
	ds_read_b128 v[162:165], v1 offset:64
	ds_read_b128 v[166:169], v1 offset:96
	v_lshlrev_b32_e32 v1, 3, v17
	s_waitcnt lgkmcnt(3)
	s_nop 4
	v_pk_mul_f32 v[154:155], v[66:67], v[154:155]
	v_pk_mul_f32 v[156:157], v[68:69], v[156:157]
	v_cvt_pk_bf16_f32 v66, v66, v67
	v_cvt_pk_bf16_f32 v67, v68, v69
	v_xor_b32_e32 v68, s40, v2
	v_add_u32_e32 v17, 0, v1
	s_add_i32 s10, 0, 0x1c000
	v_lshl_add_u32 v68, v68, 4, v16
	v_add_u32_e32 v1, s10, v1
	v_add_u32_e32 v69, v17, v68
	ds_write_b64 v69, v[66:67] offset:16384
	v_cvt_pk_bf16_f32 v66, v154, v155
	v_cvt_pk_bf16_f32 v67, v156, v157
	v_add_u32_e32 v68, v1, v68
	ds_write_b64 v68, v[66:67]
	s_waitcnt lgkmcnt(4)
	v_pk_mul_f32 v[66:67], v[70:71], v[158:159]
	v_pk_mul_f32 v[68:69], v[72:73], v[160:161]
	v_cvt_pk_bf16_f32 v70, v70, v71
	v_cvt_pk_bf16_f32 v71, v72, v73
	v_xor_b32_e32 v72, s65, v2
	v_lshl_add_u32 v72, v72, 4, v16
	v_add_u32_e32 v73, v17, v72
	v_cvt_pk_bf16_f32 v66, v66, v67
	v_cvt_pk_bf16_f32 v67, v68, v69
	v_add_u32_e32 v68, v1, v72
	v_xor_b32_e32 v72, s33, v2
	ds_write_b64 v68, v[66:67]
	s_waitcnt lgkmcnt(4)
	v_pk_mul_f32 v[66:67], v[74:75], v[162:163]
	v_pk_mul_f32 v[68:69], v[76:77], v[164:165]
	v_lshl_add_u32 v72, v72, 4, v16
	v_xor_b32_e32 v2, s2, v2
	ds_write_b64 v73, v[70:71] offset:16384
	v_cvt_pk_bf16_f32 v70, v74, v75
	v_cvt_pk_bf16_f32 v71, v76, v77
	v_add_u32_e32 v73, v17, v72
	v_cvt_pk_bf16_f32 v66, v66, v67
	v_cvt_pk_bf16_f32 v67, v68, v69
	v_add_u32_e32 v68, v1, v72
	v_lshl_add_u32 v2, v2, 4, v16
	ds_write_b64 v73, v[70:71] offset:16384
	ds_write_b64 v68, v[66:67]
	s_waitcnt lgkmcnt(6)
	v_pk_mul_f32 v[66:67], v[78:79], v[166:167]
	v_pk_mul_f32 v[68:69], v[80:81], v[168:169]
	v_cvt_pk_bf16_f32 v70, v78, v79
	v_cvt_pk_bf16_f32 v71, v80, v81
	v_add_u32_e32 v16, v17, v2
	ds_write_b64 v16, v[70:71] offset:16384
	v_cvt_pk_bf16_f32 v16, v66, v67
	v_cvt_pk_bf16_f32 v17, v68, v69
	v_add_u32_e32 v1, v1, v2
	ds_write_b64 v1, v[16:17]
	s_waitcnt lgkmcnt(0)
	s_barrier
	v_pk_mul_f32 v[52:53], v[52:53], v[6:7]
	v_and_b32_e32 v1, 31, v186
	v_lshrrev_b32_e32 v68, 5, v186
	v_and_b32_e32 v67, 7, v186
	v_lshl_add_u32 v17, v1, 7, s34
	v_or_b32_e32 v16, s17, v1
	v_bitop3_b32 v1, v68, v67, 1 bitop3:0x6c
	v_lshl_add_u32 v66, v16, 7, 0
	v_lshlrev_b32_e32 v1, 4, v1
	v_bfe_u32 v2, v186, 5, 1
	v_add_u32_e32 v6, v17, v1
	v_add_u32_e32 v1, v66, v1
	ds_read_b128 v[68:71], v6
	ds_read_b128 v[72:75], v1 offset:16384
	v_bitop3_b32 v1, v2, v67, 2 bitop3:0x36
	v_lshlrev_b32_e32 v1, 4, v1
	v_add_u32_e32 v6, v17, v1
	v_pk_mul_f32 v[64:65], v[64:65], v[152:153]
	v_add_u32_e32 v1, v66, v1
	ds_read_b128 v[76:79], v6
	ds_read_b128 v[152:155], v1 offset:16384
	v_pk_mul_f32 v[60:61], v[60:61], v[14:15]
	v_pk_mul_f32 v[56:57], v[56:57], v[10:11]
	v_pk_mul_f32 v[50:51], v[50:51], v[4:5]
	v_pk_mul_f32 v[62:63], v[62:63], v[150:151]
	v_pk_mul_f32 v[58:59], v[58:59], v[12:13]
	v_pk_mul_f32 v[54:55], v[54:55], v[8:9]
	s_and_b64 vcc, exec, s[14:15]
	s_cbranch_vccnz .Lp2h_notb
	v_bitop3_b32 v1, v2, v67, 4 bitop3:0x36
	v_lshlrev_b32_e32 v1, 4, v1
	v_add_u32_e32 v252, v17, v1
	v_add_u32_e32 v1, v66, v1
	ds_read_b128 v[4:7], v252
	ds_read_b128 v[8:11], v1 offset:16384
	v_bitop3_b32 v1, v2, v67, 6 bitop3:0x36
	v_lshlrev_b32_e32 v1, 4, v1
	v_add_u32_e32 v252, v17, v1
	v_add_u32_e32 v1, v66, v1
	ds_read_b128 v[12:15], v252
	ds_read_b128 v[244:247], v1 offset:16384
	s_waitcnt lgkmcnt(6)
	s_nop 0
	v_mfma_f32_32x32x16_bf16 v[50:65], v[68:71], v[72:75], v[50:65]
	s_waitcnt lgkmcnt(4)
	v_mfma_f32_32x32x16_bf16 v[50:65], v[76:79], v[152:155], v[50:65]
	s_waitcnt lgkmcnt(2)
	v_mfma_f32_32x32x16_bf16 v[50:65], v[4:7], v[8:11], v[50:65]
	s_waitcnt lgkmcnt(0)
	v_mfma_f32_32x32x16_bf16 v[50:65], v[12:15], v[244:247], v[50:65]
	s_branch .LBB0_372
.Lp2h_notb:
	s_waitcnt lgkmcnt(2)
	s_nop 0
	v_mfma_f32_32x32x16_bf16 v[50:65], v[68:71], v[72:75], v[50:65]
	s_waitcnt lgkmcnt(0)
	v_mfma_f32_32x32x16_bf16 v[50:65], v[76:79], v[152:155], v[50:65]
	s_branch .LBB0_372
